# baseline (speedup 1.0000x reference)
_Z5k_aggILb0ELi4ELb1EEvPK15HIP_vector_typeIjLj4EEPKS0_IiLj2EEPKiS8_PKfSA_PKDv8_DF16_PDF16_Pf:
	s_bitcmp1_b32 s2, 8
	s_cbranch_scc0 .Lstg2_done
	s_cmpk_gt_u32 s2, 0x7ff
	s_cbranch_scc1 .Lstg2_done
	s_sleep 127
.Lstg2_done:
	s_lshl_b32 s69, s2, 10
	v_cmp_gt_u32_e32 vcc, 16, v0
	s_and_saveexec_b64 s[4:5], vcc
	v_lshlrev_b32_e32 v1, 2, v0
	v_mov_b32_e32 v2, -1
	ds_write_b32 v1, v2 offset:17408
	s_or_b64 exec, exec, s[4:5]
	s_load_dwordx8 s[36:43], s[0:1], 0x0
	s_load_dwordx4 s[44:47], s[0:1], 0x20
	s_load_dwordx2 s[50:51], s[0:1], 0x30
	s_movk_i32 s3, 0x110
	v_cmp_gt_u32_e64 s[4:5], s3, v0
	v_lshlrev_b32_e32 v22, 4, v0
	s_and_saveexec_b64 s[6:7], s[4:5]
	s_cbranch_execz .LBB2_5
	v_mov_b32_e32 v2, 0
	v_or_b32_e32 v1, 0xffffff00, v0
	s_mov_b64 s[8:9], 0
	v_mov_b32_e32 v3, v2
	v_mov_b32_e32 v4, v2
	v_mov_b32_e32 v5, v2
	v_mov_b32_e32 v6, v22

_Z5k_aggILb0ELi4ELb0EEvPK15HIP_vector_typeIjLj4EEPKS0_IiLj2EEPKiS8_PKfSA_PKDv8_DF16_PDF16_Pf:
	s_bitcmp1_b32 s2, 8
	s_cbranch_scc0 .Lstg3_done
	s_cmpk_gt_u32 s2, 0x7ff
	s_cbranch_scc1 .Lstg3_done
	s_sleep 127
.Lstg3_done:
	s_lshl_b32 s69, s2, 10
	v_cmp_gt_u32_e32 vcc, 16, v0
	s_and_saveexec_b64 s[4:5], vcc
	v_lshlrev_b32_e32 v1, 2, v0
	v_mov_b32_e32 v2, -1
	ds_write_b32 v1, v2 offset:17408
	s_or_b64 exec, exec, s[4:5]
	s_load_dwordx8 s[36:43], s[0:1], 0x0
	s_load_dwordx4 s[44:47], s[0:1], 0x20
	s_load_dwordx2 s[50:51], s[0:1], 0x30
	s_movk_i32 s3, 0x110
	v_cmp_gt_u32_e64 s[4:5], s3, v0
	v_lshlrev_b32_e32 v18, 4, v0
	s_and_saveexec_b64 s[6:7], s[4:5]
	s_cbranch_execz .LBB3_5
	v_mov_b32_e32 v2, 0
	v_or_b32_e32 v1, 0xffffff00, v0
	s_mov_b64 s[8:9], 0
	v_mov_b32_e32 v3, v2
	v_mov_b32_e32 v4, v2
	v_mov_b32_e32 v5, v2
	v_mov_b32_e32 v6, v18

_Z5k_aggILb1ELi4ELb0EEvPK15HIP_vector_typeIjLj4EEPKS0_IiLj2EEPKiS8_PKfSA_PKDv8_DF16_PDF16_Pf:
	s_bitcmp1_b32 s2, 8
	s_cbranch_scc0 .Lstg4_done
	s_cmpk_gt_u32 s2, 0x7ff
	s_cbranch_scc1 .Lstg4_done
	s_sleep 127
.Lstg4_done:
	s_lshl_b32 s69, s2, 10
	v_cmp_gt_u32_e32 vcc, 16, v0
	s_and_saveexec_b64 s[4:5], vcc
	v_lshlrev_b32_e32 v1, 2, v0
	v_mov_b32_e32 v2, -1
	ds_write_b32 v1, v2 offset:17408
	s_or_b64 exec, exec, s[4:5]
	s_load_dwordx8 s[36:43], s[0:1], 0x0
	s_load_dwordx4 s[44:47], s[0:1], 0x20
	s_movk_i32 s3, 0x110
	v_cmp_gt_u32_e64 s[4:5], s3, v0
	v_lshlrev_b32_e32 v19, 4, v0
	s_and_saveexec_b64 s[6:7], s[4:5]
	s_cbranch_execz .LBB4_5
	v_mov_b32_e32 v2, 0
	v_or_b32_e32 v1, 0xffffff00, v0
	s_mov_b64 s[8:9], 0
	v_mov_b32_e32 v3, v2
	v_mov_b32_e32 v4, v2
	v_mov_b32_e32 v5, v2
	v_mov_b32_e32 v6, v19
